# prologue: nt (non-temporal) policy on the read-once f32 weight / x / p loads
# speedup vs baseline: 1.0158x; 1.0060x over previous
.LBB0_78:
	s_abs_i32 s41, s39
	s_mul_hi_u32 s42, s41, s3
	s_mul_i32 s43, s42, s4
	s_sub_i32 s41, s41, s43
	s_ashr_i32 s40, s39, 31
	s_add_i32 s43, s42, 1
	s_sub_i32 s86, s41, s4
	s_cmp_ge_u32 s41, s4
	s_cselect_b32 s42, s43, s42
	s_cselect_b32 s41, s86, s41
	s_add_i32 s43, s42, 1
	s_cmp_ge_u32 s41, s4
	s_cselect_b32 s41, s43, s42
	s_xor_b32 s41, s41, s40
	s_sub_i32 s41, s41, s40
	s_lshl_b32 s86, s41, 6
	s_mul_i32 s40, s51, s41
	v_or_b32_e32 v1, s86, v75
	s_ashr_i32 s87, s86, 31
	s_add_i32 s40, s40, s38
	s_mul_i32 s42, s87, s10
	v_mad_u64_u32 v[2:3], s[88:89], v1, s10, 0
	v_add_u32_e32 v0, s40, v74
	v_add_u32_e32 v3, s42, v3
	s_waitcnt lgkmcnt(0)
	v_lshl_add_u64 v[2:3], v[2:3], 2, s[52:53]
	v_ashrrev_i32_e32 v1, 31, v0
	v_cmp_gt_i32_e32 vcc, s10, v0
	v_lshl_add_u64 v[68:69], v[0:1], 2, v[2:3]
	v_mov_b32_e32 v4, 0
	v_mov_b32_e32 v0, 0
	v_mov_b32_e32 v1, 0
	v_mov_b32_e32 v2, 0
	v_mov_b32_e32 v3, 0
	s_and_saveexec_b64 s[88:89], vcc
	s_cbranch_execz .LBB0_80
	global_load_dwordx4 v[0:3], v[68:69], off nt
.LBB0_80:
	s_or_b64 exec, exec, s[88:89]
	v_mov_b32_e32 v5, 0
	v_mov_b32_e32 v6, 0
	v_mov_b32_e32 v7, 0
	s_and_saveexec_b64 s[88:89], vcc
	s_cbranch_execz .LBB0_82
	v_lshl_add_u64 v[4:5], s[10:11], 2, v[68:69]
	global_load_dwordx4 v[4:7], v[4:5], off nt
.LBB0_82:
	s_or_b64 exec, exec, s[88:89]
	v_mov_b32_e32 v8, 0
	v_mov_b32_e32 v12, 0
	v_mov_b32_e32 v13, 0
	v_mov_b32_e32 v14, 0
	v_mov_b32_e32 v15, 0
	s_and_saveexec_b64 s[88:89], vcc
	s_cbranch_execz .LBB0_84
	v_lshl_add_u64 v[10:11], v[68:69], 0, s[58:59]
	global_load_dwordx4 v[12:15], v[10:11], off nt
.LBB0_84:
	s_or_b64 exec, exec, s[88:89]
	v_mov_b32_e32 v9, 0
	v_mov_b32_e32 v10, 0
	v_mov_b32_e32 v11, 0
	s_and_saveexec_b64 s[88:89], vcc
	s_cbranch_execz .LBB0_86
	v_lshl_add_u64 v[8:9], v[68:69], 0, s[60:61]
	global_load_dwordx4 v[8:11], v[8:9], off nt
.LBB0_86:
	s_or_b64 exec, exec, s[88:89]
	v_mov_b32_e32 v16, 0
	v_mov_b32_e32 v20, 0
	v_mov_b32_e32 v21, 0
	v_mov_b32_e32 v22, 0
	v_mov_b32_e32 v23, 0
	s_and_saveexec_b64 s[88:89], vcc
	s_cbranch_execz .LBB0_88
	v_lshl_add_u64 v[18:19], v[68:69], 0, s[62:63]
	global_load_dwordx4 v[20:23], v[18:19], off nt
.LBB0_88:
	s_or_b64 exec, exec, s[88:89]
	v_mov_b32_e32 v17, 0
	v_mov_b32_e32 v18, 0
	v_mov_b32_e32 v19, 0
	s_and_saveexec_b64 s[88:89], vcc
	s_cbranch_execz .LBB0_90
	v_lshl_add_u64 v[16:17], v[68:69], 0, s[64:65]
	global_load_dwordx4 v[16:19], v[16:17], off nt
.LBB0_90:
	s_or_b64 exec, exec, s[88:89]
	v_mov_b32_e32 v24, 0
	v_mov_b32_e32 v28, 0
	v_mov_b32_e32 v29, 0
	v_mov_b32_e32 v30, 0
	v_mov_b32_e32 v31, 0
	s_and_saveexec_b64 s[88:89], vcc
	s_cbranch_execz .LBB0_92
	v_lshl_add_u64 v[26:27], v[68:69], 0, s[66:67]
	global_load_dwordx4 v[28:31], v[26:27], off nt
.LBB0_92:
	s_or_b64 exec, exec, s[88:89]
	v_mov_b32_e32 v25, 0
	v_mov_b32_e32 v26, 0
	v_mov_b32_e32 v27, 0
	s_and_saveexec_b64 s[88:89], vcc
	s_cbranch_execz .LBB0_94
	v_lshl_add_u64 v[24:25], v[68:69], 0, s[68:69]
	global_load_dwordx4 v[24:27], v[24:25], off nt
.LBB0_94:
	s_or_b64 exec, exec, s[88:89]
	v_mov_b32_e32 v32, 0
	v_mov_b32_e32 v36, 0
	v_mov_b32_e32 v37, 0
	v_mov_b32_e32 v38, 0
	v_mov_b32_e32 v39, 0
	s_and_saveexec_b64 s[88:89], vcc
	s_cbranch_execz .LBB0_96
	v_lshl_add_u64 v[34:35], v[68:69], 0, s[70:71]
	global_load_dwordx4 v[36:39], v[34:35], off nt
.LBB0_96:
	s_or_b64 exec, exec, s[88:89]
	v_mov_b32_e32 v33, 0
	v_mov_b32_e32 v34, 0
	v_mov_b32_e32 v35, 0
	s_and_saveexec_b64 s[88:89], vcc
	s_cbranch_execz .LBB0_98
	v_lshl_add_u64 v[32:33], v[68:69], 0, s[72:73]
	global_load_dwordx4 v[32:35], v[32:33], off nt
.LBB0_98:
	s_or_b64 exec, exec, s[88:89]
	v_mov_b32_e32 v40, 0
	v_mov_b32_e32 v44, 0
	v_mov_b32_e32 v45, 0
	v_mov_b32_e32 v46, 0
	v_mov_b32_e32 v47, 0
	s_and_saveexec_b64 s[88:89], vcc
	s_cbranch_execz .LBB0_100
	v_lshl_add_u64 v[42:43], v[68:69], 0, s[74:75]
	global_load_dwordx4 v[44:47], v[42:43], off nt
.LBB0_100:
	s_or_b64 exec, exec, s[88:89]
	v_mov_b32_e32 v41, 0
	v_mov_b32_e32 v42, 0
	v_mov_b32_e32 v43, 0
	s_and_saveexec_b64 s[88:89], vcc
	s_cbranch_execz .LBB0_102
	v_lshl_add_u64 v[40:41], v[68:69], 0, s[76:77]
	global_load_dwordx4 v[40:43], v[40:41], off nt
.LBB0_102:
	s_or_b64 exec, exec, s[88:89]
	v_mov_b32_e32 v48, 0
	v_mov_b32_e32 v52, 0
	v_mov_b32_e32 v53, 0
	v_mov_b32_e32 v54, 0
	v_mov_b32_e32 v55, 0
	s_and_saveexec_b64 s[88:89], vcc
	s_cbranch_execz .LBB0_104
	v_lshl_add_u64 v[50:51], v[68:69], 0, s[78:79]
	global_load_dwordx4 v[52:55], v[50:51], off nt
.LBB0_104:
	s_or_b64 exec, exec, s[88:89]
	v_mov_b32_e32 v49, 0
	v_mov_b32_e32 v50, 0
	v_mov_b32_e32 v51, 0
	s_and_saveexec_b64 s[88:89], vcc
	s_cbranch_execz .LBB0_106
	v_lshl_add_u64 v[48:49], v[68:69], 0, s[80:81]
	global_load_dwordx4 v[48:51], v[48:49], off nt
.LBB0_106:
	s_or_b64 exec, exec, s[88:89]
	v_mov_b32_e32 v56, 0
	v_mov_b32_e32 v60, 0
	v_mov_b32_e32 v61, 0
	v_mov_b32_e32 v62, 0
	v_mov_b32_e32 v63, 0
	s_and_saveexec_b64 s[88:89], vcc
	s_cbranch_execz .LBB0_108
	v_lshl_add_u64 v[58:59], v[68:69], 0, s[82:83]
	global_load_dwordx4 v[60:63], v[58:59], off nt
.LBB0_108:
	s_or_b64 exec, exec, s[88:89]
	v_mov_b32_e32 v57, 0
	v_mov_b32_e32 v58, 0
	v_mov_b32_e32 v59, 0
	s_and_saveexec_b64 s[88:89], vcc
	s_cbranch_execz .LBB0_110
	v_lshl_add_u64 v[56:57], v[68:69], 0, s[84:85]
	global_load_dwordx4 v[56:59], v[56:57], off nt

.LBB0_117:
	s_abs_i32 s3, s33
	s_mul_hi_u32 s38, s3, s67
	s_mul_i32 s39, s38, s4
	s_sub_i32 s3, s3, s39
	s_ashr_i32 s2, s33, 31
	s_add_i32 s39, s38, 1
	s_sub_i32 s40, s3, s4
	s_cmp_ge_u32 s3, s4
	s_cselect_b32 s38, s39, s38
	s_cselect_b32 s3, s40, s3
	s_add_i32 s39, s38, 1
	s_cmp_ge_u32 s3, s4
	s_cselect_b32 s3, s39, s38
	s_xor_b32 s3, s3, s2
	s_sub_i32 s70, s3, s2
	s_mul_i32 s2, s64, s70
	s_add_i32 s71, s33, s2
	s_mul_i32 s2, s66, s70
	s_lshl_b32 s60, s70, 7
	s_add_i32 s69, s68, s2
	v_add_u32_e32 v0, s69, v74
	s_cmpk_lt_i32 s71, 0x58
	s_cselect_b64 s[62:63], -1, 0
	v_or_b32_e32 v48, s60, v76
	v_ashrrev_i32_e32 v1, 31, v0
	s_ashr_i32 s61, s60, 31
	s_waitcnt lgkmcnt(0)
	v_lshl_add_u64 v[36:37], v[0:1], 2, s[52:53]
	s_mul_i32 s2, s61, s10
	v_mad_u64_u32 v[0:1], s[38:39], v48, s10, 0
	v_add_u32_e32 v1, s2, v1
	v_lshl_add_u64 v[0:1], v[0:1], 2, v[36:37]
	global_load_dwordx4 v[24:27], v[0:1], off nt
	v_lshl_add_u64 v[0:1], v[0:1], 0, s[0:1]
	global_load_dwordx4 v[32:35], v[0:1], off nt
	v_lshl_add_u64 v[0:1], v[0:1], 0, s[0:1]
	global_load_dwordx4 v[40:43], v[0:1], off nt
	v_lshl_add_u64 v[0:1], v[0:1], 0, s[0:1]
	global_load_dwordx4 v[44:47], v[0:1], off nt
	v_lshl_add_u64 v[0:1], v[0:1], 0, s[58:59]
	v_lshl_add_u64 v[2:3], v[0:1], 0, s[0:1]
	global_load_dwordx4 v[12:15], v[0:1], off nt
	global_load_dwordx4 v[8:11], v[2:3], off nt
	v_lshl_add_u64 v[0:1], v[2:3], 0, s[0:1]
	v_lshl_add_u64 v[16:17], v[0:1], 0, s[0:1]
	global_load_dwordx4 v[4:7], v[0:1], off nt
	s_nop 0
	global_load_dwordx4 v[0:3], v[16:17], off nt
	v_lshl_add_u64 v[16:17], v[16:17], 0, s[58:59]
	v_lshl_add_u64 v[20:21], v[16:17], 0, s[0:1]
	s_and_b64 vcc, s[56:57], s[62:63]
	global_load_dwordx4 v[28:31], v[16:17], off nt
	v_cndmask_b32_e32 v52, v89, v50, vcc
	global_load_dwordx4 v[16:19], v[20:21], off nt
	v_lshl_add_u64 v[38:39], v[20:21], 0, s[0:1]
	global_load_dwordx4 v[20:23], v[38:39], off nt
	v_lshl_add_u64 v[38:39], v[38:39], 0, s[0:1]
	v_mov_b32_e32 v53, 0
	v_mov_b32_e32 v68, 0
	v_mov_b32_e32 v69, 0
	v_mov_b32_e32 v90, 0
	v_mov_b32_e32 v54, 0
	v_mov_b32_e32 v91, 0
	v_add_u32_e32 v51, v77, v78
	s_andn2_b64 vcc, exec, s[56:57]
	s_waitcnt vmcnt(10)
	v_mul_f32_e32 v55, v24, v52
	v_mul_f32_e32 v56, v25, v52
	s_waitcnt vmcnt(9)
	v_mul_f32_e32 v59, v32, v52
	v_or_b32_e32 v32, 64, v48
	v_mul_f32_e32 v60, v33, v52
	v_mad_u64_u32 v[32:33], s[38:39], v32, s10, 0
	v_add_u32_e32 v33, s2, v33
	v_mul_f32_e32 v57, v26, v52
	v_mul_f32_e32 v58, v27, v52
	global_load_dwordx4 v[24:27], v[38:39], off nt
	v_lshl_add_u64 v[48:49], v[32:33], 2, v[36:37]
	v_lshl_add_u64 v[32:33], v[38:39], 0, s[58:59]
	v_mul_f32_e32 v34, v34, v52
	v_cvt_pk_fp8_f32 v53, v55, v59
	global_load_dwordx4 v[36:39], v[32:33], off nt
	v_lshl_add_u64 v[32:33], v[32:33], 0, s[0:1]
	v_cvt_pk_fp8_f32 v68, v56, v60
	v_cvt_pk_fp8_f32 v69, v57, v34
	s_waitcnt vmcnt(9)
	v_mul_f32_e32 v34, v52, v44
	v_mul_f32_e32 v59, v52, v45
	v_mul_f32_e32 v60, v52, v46
	v_mul_f32_e32 v61, v52, v47
	global_load_dwordx4 v[44:47], v[32:33], off nt
	v_mul_f32_e32 v40, v40, v52
	v_lshl_add_u64 v[32:33], v[32:33], 0, s[0:1]
	v_mul_f32_e32 v35, v35, v52
	v_mul_f32_e32 v55, v41, v52
	v_mul_f32_e32 v56, v42, v52
	v_mul_f32_e32 v57, v43, v52
	v_cvt_pk_fp8_f32 v53, v40, v34 op_sel:[0,0,1]
	global_load_dwordx4 v[40:43], v[32:33], off nt
	v_lshl_add_u64 v[32:33], v[32:33], 0, s[0:1]
	v_cvt_pk_fp8_f32 v90, v58, v35
	global_load_dwordx4 v[32:35], v[32:33], off nt
	s_waitcnt vmcnt(11)
	v_mul_f32_e32 v12, v52, v12
	s_waitcnt vmcnt(10)
	v_mul_f32_e32 v8, v52, v8
	v_cvt_pk_fp8_f32 v54, v12, v8
	s_waitcnt vmcnt(9)
	v_mul_f32_e32 v4, v52, v4
	s_waitcnt vmcnt(8)
	v_mul_f32_e32 v0, v52, v0
	v_mov_b32_e32 v8, 0
	v_cvt_pk_fp8_f32 v54, v4, v0 op_sel:[0,0,1]
	v_mul_f32_e32 v0, v52, v13
	v_mul_f32_e32 v4, v52, v9
	v_cvt_pk_fp8_f32 v91, v0, v4
	v_mul_f32_e32 v0, v52, v14
	v_mul_f32_e32 v4, v52, v5
	v_mul_f32_e32 v5, v52, v10
	v_cvt_pk_fp8_f32 v8, v0, v5
	v_mul_f32_e32 v0, v52, v1
	v_cvt_pk_fp8_f32 v91, v4, v0 op_sel:[0,0,1]
	v_mul_f32_e32 v0, v52, v6
	v_mul_f32_e32 v1, v52, v2
	v_cvt_pk_fp8_f32 v68, v55, v59 op_sel:[0,0,1]
	v_cvt_pk_fp8_f32 v69, v56, v60 op_sel:[0,0,1]
	ds_write2_b32 v51, v53, v54 offset1:4
	v_cvt_pk_fp8_f32 v8, v0, v1 op_sel:[0,0,1]
	v_lshl_add_u64 v[62:63], v[48:49], 0, s[0:1]
	v_cvt_pk_fp8_f32 v90, v57, v61 op_sel:[0,0,1]
	global_load_dwordx4 v[54:57], v[48:49], off nt
	global_load_dwordx4 v[58:61], v[62:63], off nt
	v_lshl_add_u64 v[0:1], v[62:63], 0, s[0:1]
	ds_write2_b32 v51, v68, v91 offset0:33 offset1:37
	ds_write2_b32 v51, v69, v8 offset0:66 offset1:70
	v_mul_f32_e32 v2, v52, v15
	v_lshl_add_u64 v[4:5], v[0:1], 0, s[0:1]
	v_mul_f32_e32 v6, v52, v11
	global_load_dwordx4 v[8:11], v[0:1], off nt
	global_load_dwordx4 v[12:15], v[4:5], off nt
	v_mov_b32_e32 v53, 0
	v_cvt_pk_fp8_f32 v53, v2, v6
	v_mul_f32_e32 v2, v52, v7
	v_mul_f32_e32 v3, v52, v3
	v_lshl_add_u64 v[0:1], v[4:5], 0, s[58:59]
	v_cvt_pk_fp8_f32 v53, v2, v3 op_sel:[0,0,1]
	v_lshl_add_u64 v[48:49], v[0:1], 0, s[0:1]
	s_waitcnt vmcnt(11)
	v_mul_f32_e32 v2, v52, v28
	s_waitcnt vmcnt(10)
	v_mul_f32_e32 v3, v52, v16
	v_mov_b32_e32 v62, 0
	v_cvt_pk_fp8_f32 v62, v2, v3
	v_mul_f32_e32 v16, v52, v29
	global_load_dwordx4 v[0:3], v[0:1], off nt
	s_nop 0
	global_load_dwordx4 v[4:7], v[48:49], off nt
	v_lshl_add_u64 v[28:29], v[48:49], 0, s[0:1]
	v_mul_f32_e32 v17, v52, v17
	v_mov_b32_e32 v48, 0
	v_mul_f32_e32 v30, v52, v30
	ds_write2_b32 v51, v90, v53 offset0:99 offset1:103
	v_cvt_pk_fp8_f32 v48, v16, v17
	v_mul_f32_e32 v16, v52, v18
	v_mov_b32_e32 v53, 0
	v_cvt_pk_fp8_f32 v53, v30, v16
	s_waitcnt vmcnt(11)
	v_mul_f32_e32 v20, v52, v20
	s_waitcnt vmcnt(10)
	v_mul_f32_e32 v24, v52, v24
	v_mul_f32_e32 v16, v52, v21
	v_mul_f32_e32 v17, v52, v25
	v_mul_f32_e32 v31, v52, v31
	v_cvt_pk_fp8_f32 v62, v20, v24 op_sel:[0,0,1]
	v_cvt_pk_fp8_f32 v48, v16, v17 op_sel:[0,0,1]
	v_mul_f32_e32 v16, v52, v22
	v_mul_f32_e32 v17, v52, v26
	v_lshl_add_u64 v[24:25], v[28:29], 0, s[0:1]
	v_mul_f32_e32 v26, v52, v19
	v_mov_b32_e32 v63, 0
	v_cvt_pk_fp8_f32 v53, v16, v17 op_sel:[0,0,1]
	v_mul_f32_e32 v30, v52, v23
	global_load_dwordx4 v[16:19], v[28:29], off nt
	global_load_dwordx4 v[20:23], v[24:25], off nt
	v_lshl_add_u64 v[28:29], v[24:25], 0, s[58:59]
	v_mul_f32_e32 v24, v52, v27
	v_cvt_pk_fp8_f32 v63, v31, v26
	s_waitcnt vmcnt(11)
	v_mul_f32_e32 v25, v52, v36
	s_waitcnt vmcnt(10)
	v_mul_f32_e32 v26, v52, v44
	v_mov_b32_e32 v27, 0
	v_cvt_pk_fp8_f32 v27, v25, v26
	v_cvt_pk_fp8_f32 v63, v30, v24 op_sel:[0,0,1]
	s_waitcnt vmcnt(9)
	v_mul_f32_e32 v24, v52, v40
	v_mov_b32_e32 v36, 0
	s_waitcnt vmcnt(8)
	v_mul_f32_e32 v25, v52, v32
	v_cvt_pk_fp8_f32 v27, v24, v25 op_sel:[0,0,1]
	v_mul_f32_e32 v24, v52, v37
	v_mul_f32_e32 v25, v52, v45
	v_cvt_pk_fp8_f32 v36, v24, v25
	v_mul_f32_e32 v24, v52, v41
	v_mul_f32_e32 v25, v52, v33
	v_lshl_add_u64 v[32:33], v[28:29], 0, s[0:1]
	v_cvt_pk_fp8_f32 v36, v24, v25 op_sel:[0,0,1]
	v_mul_f32_e32 v24, v52, v38
	v_mul_f32_e32 v25, v52, v46
	v_mov_b32_e32 v46, 0
	v_cvt_pk_fp8_f32 v46, v24, v25
	ds_write2_b32 v51, v62, v27 offset0:8 offset1:12
	global_load_dwordx4 v[24:27], v[28:29], off nt
	ds_write2_b32 v51, v48, v36 offset0:41 offset1:45
	global_load_dwordx4 v[28:31], v[32:33], off nt
	v_mul_f32_e32 v36, v52, v42
	v_mul_f32_e32 v34, v52, v34
	v_cvt_pk_fp8_f32 v46, v36, v34 op_sel:[0,0,1]
	v_lshl_add_u64 v[32:33], v[32:33], 0, s[0:1]
	v_mul_f32_e32 v49, v52, v39
	global_load_dwordx4 v[36:39], v[32:33], off nt
	v_lshl_add_u64 v[32:33], v[32:33], 0, s[0:1]
	v_mul_f32_e32 v34, v52, v47
	v_lshl_add_u64 v[44:45], v[32:33], 0, s[58:59]
	v_mov_b32_e32 v68, 0
	v_mul_f32_e32 v47, v52, v43
	global_load_dwordx4 v[40:43], v[32:33], off nt
	v_mul_f32_e32 v62, v52, v35
	v_cvt_pk_fp8_f32 v68, v49, v34
	global_load_dwordx4 v[32:35], v[44:45], off nt
	v_lshl_add_u64 v[48:49], v[44:45], 0, s[0:1]
	ds_write2_b32 v51, v53, v46 offset0:74 offset1:78
	s_waitcnt vmcnt(12)
	v_mul_f32_e32 v44, v52, v54
	s_waitcnt vmcnt(11)
	v_mul_f32_e32 v45, v52, v58
	v_mov_b32_e32 v53, 0
	v_cvt_pk_fp8_f32 v53, v44, v45
	s_waitcnt vmcnt(10)
	v_mul_f32_e32 v8, v52, v8
	s_waitcnt vmcnt(9)
	v_mul_f32_e32 v12, v52, v12
	v_mul_f32_e32 v54, v52, v55
	v_cvt_pk_fp8_f32 v53, v8, v12 op_sel:[0,0,1]
	v_mul_f32_e32 v8, v52, v59
	v_mov_b32_e32 v12, 0
	v_cvt_pk_fp8_f32 v68, v47, v62 op_sel:[0,0,1]
	v_mul_f32_e32 v55, v52, v56
	v_cvt_pk_fp8_f32 v12, v54, v8
	v_mul_f32_e32 v8, v52, v60
	v_mov_b32_e32 v62, 0
	global_load_dwordx4 v[44:47], v[48:49], off nt
	v_cvt_pk_fp8_f32 v62, v55, v8
	v_mul_f32_e32 v8, v52, v9
	v_mul_f32_e32 v9, v52, v13
	v_lshl_add_u64 v[48:49], v[48:49], 0, s[0:1]
	v_cvt_pk_fp8_f32 v12, v8, v9 op_sel:[0,0,1]
	v_mul_f32_e32 v8, v52, v10
	v_mul_f32_e32 v9, v52, v14
	v_mul_f32_e32 v58, v52, v57
	v_cvt_pk_fp8_f32 v62, v8, v9 op_sel:[0,0,1]
	v_mul_f32_e32 v10, v52, v61
	v_lshl_add_u64 v[8:9], v[48:49], 0, s[0:1]
	v_mov_b32_e32 v13, 0
	global_load_dwordx4 v[54:57], v[48:49], off nt
	v_cvt_pk_fp8_f32 v13, v58, v10
	global_load_dwordx4 v[58:61], v[8:9], off nt
	s_waitcnt vmcnt(11)
	v_mul_f32_e32 v0, v52, v0
	s_waitcnt vmcnt(10)
	v_mul_f32_e32 v4, v52, v4
	v_mov_b32_e32 v10, 0
	v_cvt_pk_fp8_f32 v10, v0, v4
	v_mul_f32_e32 v0, v52, v1
	v_mul_f32_e32 v1, v52, v5
	v_mov_b32_e32 v4, 0
	v_cvt_pk_fp8_f32 v4, v0, v1
	s_waitcnt vmcnt(9)
	v_mul_f32_e32 v0, v52, v17
	s_waitcnt vmcnt(8)
	v_mul_f32_e32 v1, v52, v21
	v_mul_f32_e32 v8, v52, v11
	v_cvt_pk_fp8_f32 v4, v0, v1 op_sel:[0,0,1]
	v_mul_f32_e32 v0, v52, v2
	v_mul_f32_e32 v1, v52, v6
	v_mov_b32_e32 v6, 0
	v_mul_f32_e32 v9, v52, v15
	v_cvt_pk_fp8_f32 v6, v0, v1
	v_mul_f32_e32 v0, v52, v3
	v_mul_f32_e32 v1, v52, v7
	v_mov_b32_e32 v3, 0
	v_cvt_pk_fp8_f32 v13, v8, v9 op_sel:[0,0,1]
	v_mul_f32_e32 v8, v52, v16
	v_mul_f32_e32 v9, v52, v20
	v_cvt_pk_fp8_f32 v3, v0, v1
	v_cvt_pk_fp8_f32 v10, v8, v9 op_sel:[0,0,1]
	v_mul_f32_e32 v2, v52, v18
	v_mul_f32_e32 v5, v52, v22
	v_cvt_pk_fp8_f32 v6, v2, v5 op_sel:[0,0,1]
	v_mul_f32_e32 v0, v52, v19
	v_mul_f32_e32 v1, v52, v23
	v_cvt_pk_fp8_f32 v3, v0, v1 op_sel:[0,0,1]
	ds_write2_b32 v51, v63, v68 offset0:107 offset1:111
	ds_write2_b32 v51, v53, v10 offset0:16 offset1:20
	ds_write2_b32 v51, v12, v4 offset0:49 offset1:53
	ds_write2_b32 v51, v62, v6 offset0:82 offset1:86
	ds_write2_b32 v51, v13, v3 offset0:115 offset1:119
	s_waitcnt vmcnt(7)
	v_mul_f32_e32 v0, v52, v24
	s_waitcnt vmcnt(6)
	v_mul_f32_e32 v1, v52, v28
	v_mov_b32_e32 v4, 0
	v_cvt_pk_fp8_f32 v4, v0, v1
	v_mul_f32_e32 v0, v52, v25
	v_mul_f32_e32 v1, v52, v29
	v_mov_b32_e32 v5, 0
	v_cvt_pk_fp8_f32 v5, v0, v1
	s_waitcnt vmcnt(5)
	v_mul_f32_e32 v0, v52, v37
	v_mov_b32_e32 v6, 0
	s_waitcnt vmcnt(4)
	v_mul_f32_e32 v1, v52, v41
	v_cvt_pk_fp8_f32 v5, v0, v1 op_sel:[0,0,1]
	v_mul_f32_e32 v0, v52, v26
	v_mul_f32_e32 v1, v52, v30
	v_cvt_pk_fp8_f32 v6, v0, v1
	v_mul_f32_e32 v0, v52, v27
	v_mul_f32_e32 v1, v52, v31
	v_mov_b32_e32 v7, 0
	v_cvt_pk_fp8_f32 v7, v0, v1
	v_mul_f32_e32 v0, v52, v39
	v_mul_f32_e32 v1, v52, v43
	v_mov_b32_e32 v8, 0
	v_cvt_pk_fp8_f32 v7, v0, v1 op_sel:[0,0,1]
	s_waitcnt vmcnt(3)
	v_mul_f32_e32 v0, v52, v32
	v_mov_b32_e32 v9, 0
	v_mul_f32_e32 v2, v52, v36
	v_mul_f32_e32 v3, v52, v40
	v_mov_b32_e32 v10, 0
	v_cvt_pk_fp8_f32 v4, v2, v3 op_sel:[0,0,1]
	v_mul_f32_e32 v2, v52, v38
	v_mul_f32_e32 v3, v52, v42
	s_waitcnt vmcnt(2)
	v_mul_f32_e32 v1, v52, v44
	v_cvt_pk_fp8_f32 v8, v0, v1
	v_mul_f32_e32 v0, v52, v33
	v_mul_f32_e32 v1, v52, v45
	v_cvt_pk_fp8_f32 v9, v0, v1
	v_mov_b32_e32 v11, 0
	v_cvt_pk_fp8_f32 v6, v2, v3 op_sel:[0,0,1]
	s_waitcnt vmcnt(1)
	v_mul_f32_e32 v0, v52, v55
	v_mul_f32_e32 v2, v52, v54
	s_waitcnt vmcnt(0)
	v_mul_f32_e32 v1, v52, v59
	v_cvt_pk_fp8_f32 v9, v0, v1 op_sel:[0,0,1]
	v_mul_f32_e32 v0, v52, v34
	v_mul_f32_e32 v1, v52, v46
	v_cvt_pk_fp8_f32 v10, v0, v1
	v_mul_f32_e32 v0, v52, v35
	v_mul_f32_e32 v1, v52, v47
	v_mul_f32_e32 v3, v52, v58
	v_cvt_pk_fp8_f32 v11, v0, v1
	v_cvt_pk_fp8_f32 v8, v2, v3 op_sel:[0,0,1]
	v_mul_f32_e32 v2, v52, v56
	v_mul_f32_e32 v3, v52, v60
	v_cvt_pk_fp8_f32 v10, v2, v3 op_sel:[0,0,1]
	v_mul_f32_e32 v0, v52, v57
	v_mul_f32_e32 v1, v52, v61
	v_cvt_pk_fp8_f32 v11, v0, v1 op_sel:[0,0,1]
	ds_write2_b32 v51, v4, v8 offset0:24 offset1:28
	ds_write2_b32 v51, v5, v9 offset0:57 offset1:61
	ds_write2_b32 v51, v6, v10 offset0:90 offset1:94
	ds_write2_b32 v51, v7, v11 offset0:123 offset1:127
	s_waitcnt lgkmcnt(0)
	s_cbranch_vccnz .LBB0_116
	s_cmpk_gt_i32 s71, 0x57
	s_cselect_b32 s2, 0xffffea00, 0
	s_mul_i32 s3, s65, s70
	s_cselect_b32 s38, 0x80, 0
	s_sub_i32 s2, s2, s3
	s_add_i32 s2, s68, s2
	s_lshl_b32 s2, s2, 1
	s_and_b32 s3, s69, 64
	s_and_b32 s2, s2, 0xffffff00
	s_or_b32 s3, s3, s38
	s_or_b32 s69, s3, s2
	s_branch .LBB0_116

.LBB0_124:
	global_load_dwordx4 v[24:27], v[38:39], off offset:16 nt
	global_load_dwordx4 v[28:31], v[38:39], off nt
	v_lshl_add_u64 v[42:43], v[40:41], 0, s[12:13]
	v_cmp_gt_u64_e32 vcc, s[30:31], v[42:43]
	s_and_saveexec_b64 s[0:1], vcc
	s_cbranch_execz .LBB0_126
	v_lshl_add_u64 v[0:1], v[38:39], 0, s[14:15]
	global_load_dwordx4 v[8:11], v[0:1], off offset:16 nt
	s_nop 0
	global_load_dwordx4 v[0:3], v[0:1], off nt
.LBB0_126:
	s_or_b64 exec, exec, s[0:1]
	v_lshl_add_u64 v[44:45], s[18:19], 0, v[40:41]
	v_cmp_gt_u64_e64 s[0:1], s[30:31], v[44:45]
	s_and_saveexec_b64 s[2:3], s[0:1]
	s_cbranch_execz .LBB0_128
	v_lshl_add_u64 v[4:5], v[38:39], 0, s[24:25]
	global_load_dwordx4 v[16:19], v[4:5], off nt
	s_nop 0
	global_load_dwordx4 v[4:7], v[4:5], off offset:-16 nt
.LBB0_128:
	s_or_b64 exec, exec, s[2:3]
	v_lshl_add_u64 v[44:45], s[20:21], 0, v[40:41]
	v_cmp_gt_u64_e64 s[2:3], s[30:31], v[44:45]
	s_and_saveexec_b64 s[50:51], s[2:3]
	s_cbranch_execz .LBB0_130
	v_lshl_add_u64 v[12:13], v[38:39], 0, s[26:27]
	global_load_dwordx4 v[20:23], v[12:13], off nt
	s_nop 0
	global_load_dwordx4 v[12:15], v[12:13], off offset:-16 nt

.LBB0_139:
	global_load_dwordx4 v[24:27], v[36:37], off offset:16 nt
	global_load_dwordx4 v[28:31], v[36:37], off nt
	v_lshl_add_u64 v[38:39], v[32:33], 0, s[12:13]
	v_cmp_gt_u64_e32 vcc, s[34:35], v[38:39]
	s_and_saveexec_b64 s[0:1], vcc
	s_cbranch_execz .LBB0_141
	v_lshl_add_u64 v[0:1], v[36:37], 0, s[14:15]
	global_load_dwordx4 v[8:11], v[0:1], off offset:16 nt
	s_nop 0
	global_load_dwordx4 v[0:3], v[0:1], off nt
.LBB0_141:
	s_or_b64 exec, exec, s[0:1]
	v_lshl_add_u64 v[40:41], s[18:19], 0, v[32:33]
	v_cmp_gt_u64_e64 s[0:1], s[34:35], v[40:41]
	s_and_saveexec_b64 s[2:3], s[0:1]
	s_cbranch_execz .LBB0_143
	v_lshl_add_u64 v[4:5], v[36:37], 0, s[24:25]
	global_load_dwordx4 v[16:19], v[4:5], off nt
	s_nop 0
	global_load_dwordx4 v[4:7], v[4:5], off offset:-16 nt
.LBB0_143:
	s_or_b64 exec, exec, s[2:3]
	v_lshl_add_u64 v[32:33], s[20:21], 0, v[32:33]
	v_cmp_gt_u64_e64 s[2:3], s[34:35], v[32:33]
	s_and_saveexec_b64 s[40:41], s[2:3]
	s_cbranch_execz .LBB0_145
	v_lshl_add_u64 v[12:13], v[36:37], 0, s[26:27]
	global_load_dwordx4 v[20:23], v[12:13], off nt
	s_nop 0
	global_load_dwordx4 v[12:15], v[12:13], off offset:-16 nt
